# speedup vs baseline: 1.0135x; 1.0050x over previous
	.amdhsa_kernel _Z6k_agg1PKiS0_PK6__halfPKfS5_S5_S3_S5_S5_PS1_PfS7_S5_S0_S0_
		.amdhsa_group_segment_fixed_size 5376
		.amdhsa_private_segment_fixed_size 0
		.amdhsa_kernarg_size 120
		.amdhsa_user_sgpr_count 2
		.amdhsa_user_sgpr_dispatch_ptr 0
		.amdhsa_user_sgpr_queue_ptr 0
		.amdhsa_user_sgpr_kernarg_segment_ptr 1
		.amdhsa_user_sgpr_dispatch_id 0
		.amdhsa_user_sgpr_kernarg_preload_length 0
		.amdhsa_user_sgpr_kernarg_preload_offset 0
		.amdhsa_user_sgpr_private_segment_size 0
		.amdhsa_uses_dynamic_stack 0
		.amdhsa_enable_private_segment 0
		.amdhsa_system_sgpr_workgroup_id_x 1
		.amdhsa_system_sgpr_workgroup_id_y 0
		.amdhsa_system_sgpr_workgroup_id_z 0
		.amdhsa_system_sgpr_workgroup_info 0
		.amdhsa_system_vgpr_workitem_id 0
		.amdhsa_next_free_vgpr 96
		.amdhsa_next_free_sgpr 37
		.amdhsa_accum_offset 96
		.amdhsa_reserve_vcc 1
		.amdhsa_float_round_mode_32 0
		.amdhsa_float_round_mode_16_64 0
		.amdhsa_float_denorm_mode_32 3
		.amdhsa_float_denorm_mode_16_64 3
		.amdhsa_dx10_clamp 1
		.amdhsa_ieee_mode 1
		.amdhsa_fp16_overflow 0
		.amdhsa_tg_split 0
		.amdhsa_exception_fp_ieee_invalid_op 0
		.amdhsa_exception_fp_denorm_src 0
		.amdhsa_exception_fp_ieee_div_zero 0
		.amdhsa_exception_fp_ieee_overflow 0
		.amdhsa_exception_fp_ieee_underflow 0
		.amdhsa_exception_fp_ieee_inexact 0
		.amdhsa_exception_int_div_zero 0
	.end_amdhsa_kernel

amdhsa.kernels:
  - .agpr_count:     0
    .args:
      - .actual_access:  read_only
        .address_space:  global
        .offset:         0
        .size:           8
        .value_kind:     global_buffer
      - .actual_access:  read_only
        .address_space:  global
        .offset:         8
        .size:           8
        .value_kind:     global_buffer
      - .actual_access:  write_only
        .address_space:  global
        .offset:         16
        .size:           8
        .value_kind:     global_buffer
      - .actual_access:  write_only
        .address_space:  global
        .offset:         24
        .size:           8
        .value_kind:     global_buffer
      - .actual_access:  write_only
        .address_space:  global
        .offset:         32
        .size:           8
        .value_kind:     global_buffer
    .group_segment_fixed_size: 0
    .kernarg_segment_align: 8
    .kernarg_segment_size: 40
    .language:       OpenCL C
    .language_version:
      - 2
      - 0
    .max_flat_workgroup_size: 256
    .name:           _Z6k_prepPKfS0_P6__halfS2_Pi
    .private_segment_fixed_size: 0
    .sgpr_count:     18
    .sgpr_spill_count: 0
    .symbol:         _Z6k_prepPKfS0_P6__halfS2_Pi.kd
    .uniform_work_group_size: 1
    .uses_dynamic_stack: false
    .vgpr_count:     6
    .vgpr_spill_count: 0
    .wavefront_size: 64
  - .agpr_count:     0
    .args:
      - .actual_access:  read_only
        .address_space:  global
        .offset:         0
        .size:           8
        .value_kind:     global_buffer
      - .actual_access:  read_only
        .address_space:  global
        .offset:         8
        .size:           8
        .value_kind:     global_buffer
      - .address_space:  global
        .offset:         16
        .size:           8
        .value_kind:     global_buffer
      - .actual_access:  write_only
        .address_space:  global
        .offset:         24
        .size:           8
        .value_kind:     global_buffer
      - .actual_access:  write_only
        .address_space:  global
        .offset:         32
        .size:           8
        .value_kind:     global_buffer
      - .actual_access:  read_only
        .address_space:  global
        .offset:         40
        .size:           8
        .value_kind:     global_buffer
      - .actual_access:  read_only
        .address_space:  global
        .offset:         48
        .size:           8
        .value_kind:     global_buffer
      - .actual_access:  read_only
        .address_space:  global
        .offset:         56
        .size:           8
        .value_kind:     global_buffer
      - .actual_access:  read_only
        .address_space:  global
        .offset:         64
        .size:           8
        .value_kind:     global_buffer
      - .actual_access:  write_only
        .address_space:  global
        .offset:         72
        .size:           8
        .value_kind:     global_buffer
      - .actual_access:  read_only
        .address_space:  global
        .offset:         80
        .size:           8
        .value_kind:     global_buffer
      - .actual_access:  write_only
        .address_space:  global
        .offset:         88
        .size:           8
        .value_kind:     global_buffer
    .group_segment_fixed_size: 53248
    .kernarg_segment_align: 8
    .kernarg_segment_size: 96
    .language:       OpenCL C
    .language_version:
      - 2
      - 0
    .max_flat_workgroup_size: 256
    .name:           _Z15k_scatter_gemm1PKiS0_PiPjPyPKfPK6__halfS5_S5_PS6_PfSA_
    .private_segment_fixed_size: 0
    .sgpr_count:     32
    .sgpr_spill_count: 0
    .symbol:         _Z15k_scatter_gemm1PKiS0_PiPjPyPKfPK6__halfS5_S5_PS6_PfSA_.kd
    .uniform_work_group_size: 1
    .uses_dynamic_stack: false
    .vgpr_count:     146
    .vgpr_spill_count: 0
    .wavefront_size: 64
  - .agpr_count:     0
    .args:
      - .actual_access:  read_only
        .address_space:  global
        .offset:         0
        .size:           8
        .value_kind:     global_buffer
      - .actual_access:  read_only
        .address_space:  global
        .offset:         8
        .size:           8
        .value_kind:     global_buffer
      - .actual_access:  read_only
        .address_space:  global
        .offset:         16
        .size:           8
        .value_kind:     global_buffer
      - .actual_access:  write_only
        .address_space:  global
        .offset:         24
        .size:           8
        .value_kind:     global_buffer
      - .actual_access:  write_only
        .address_space:  global
        .offset:         32
        .size:           8
        .value_kind:     global_buffer
      - .actual_access:  write_only
        .address_space:  global
        .offset:         40
        .size:           8
        .value_kind:     global_buffer
      - .actual_access:  write_only
        .address_space:  global
        .offset:         48
        .size:           8
        .value_kind:     global_buffer
      - .actual_access:  read_only
        .address_space:  global
        .offset:         56
        .size:           8
        .value_kind:     global_buffer
      - .actual_access:  read_only
        .address_space:  global
        .offset:         64
        .size:           8
        .value_kind:     global_buffer
      - .actual_access:  read_only
        .address_space:  global
        .offset:         72
        .size:           8
        .value_kind:     global_buffer
      - .actual_access:  read_only
        .address_space:  global
        .offset:         80
        .size:           8
        .value_kind:     global_buffer
      - .actual_access:  write_only
        .address_space:  global
        .offset:         88
        .size:           8
        .value_kind:     global_buffer
      - .actual_access:  read_only
        .address_space:  global
        .offset:         96
        .size:           8
        .value_kind:     global_buffer
      - .actual_access:  write_only
        .address_space:  global
        .offset:         104
        .size:           8
        .value_kind:     global_buffer
    .group_segment_fixed_size: 53248
    .kernarg_segment_align: 8
    .kernarg_segment_size: 112
    .language:       OpenCL C
    .language_version:
      - 2
      - 0
    .max_flat_workgroup_size: 256
    .name:           _Z12k_fine_gemm1PKjPKyPKiPiS5_S5_S5_PKfPK6__halfS7_S7_PS8_PfSC_
    .private_segment_fixed_size: 0
    .sgpr_count:     102
    .sgpr_spill_count: 0
    .symbol:         _Z12k_fine_gemm1PKjPKyPKiPiS5_S5_S5_PKfPK6__halfS7_S7_PS8_PfSC_.kd
    .uniform_work_group_size: 1
    .uses_dynamic_stack: false
    .vgpr_count:     144
    .vgpr_spill_count: 0
    .wavefront_size: 64
  - .agpr_count:     0
    .args:
      - .actual_access:  read_only
        .address_space:  global
        .offset:         0
        .size:           8
        .value_kind:     global_buffer
      - .actual_access:  read_only
        .address_space:  global
        .offset:         8
        .size:           8
        .value_kind:     global_buffer
      - .actual_access:  read_only
        .address_space:  global
        .offset:         16
        .size:           8
        .value_kind:     global_buffer
      - .actual_access:  read_only
        .address_space:  global
        .offset:         24
        .size:           8
        .value_kind:     global_buffer
      - .actual_access:  read_only
        .address_space:  global
        .offset:         32
        .size:           8
        .value_kind:     global_buffer
      - .actual_access:  read_only
        .address_space:  global
        .offset:         40
        .size:           8
        .value_kind:     global_buffer
      - .actual_access:  read_only
        .address_space:  global
        .offset:         48
        .size:           8
        .value_kind:     global_buffer
      - .actual_access:  read_only
        .address_space:  global
        .offset:         56
        .size:           8
        .value_kind:     global_buffer
      - .actual_access:  read_only
        .address_space:  global
        .offset:         64
        .size:           8
        .value_kind:     global_buffer
      - .actual_access:  write_only
        .address_space:  global
        .offset:         72
        .size:           8
        .value_kind:     global_buffer
      - .actual_access:  read_only
        .address_space:  global
        .offset:         80
        .size:           8
        .value_kind:     global_buffer
      - .actual_access:  write_only
        .address_space:  global
        .offset:         88
        .size:           8
        .value_kind:     global_buffer
      - .actual_access:  read_only
        .address_space:  global
        .offset:         96
        .size:           8
        .value_kind:     global_buffer
      - .actual_access:  read_only
        .address_space:  global
        .offset:         104
        .size:           8
        .value_kind:     global_buffer
      - .actual_access:  read_only
        .address_space:  global
        .offset:         112
        .size:           8
        .value_kind:     global_buffer
    .group_segment_fixed_size: 5376
    .kernarg_segment_align: 8
    .kernarg_segment_size: 120
    .language:       OpenCL C
    .language_version:
      - 2
      - 0
    .max_flat_workgroup_size: 256
    .name:           _Z6k_agg1PKiS0_PK6__halfPKfS5_S5_S3_S5_S5_PS1_PfS7_S5_S0_S0_
    .private_segment_fixed_size: 0
    .sgpr_count:     43
    .sgpr_spill_count: 0
    .symbol:         _Z6k_agg1PKiS0_PK6__halfPKfS5_S5_S3_S5_S5_PS1_PfS7_S5_S0_S0_.kd
    .uniform_work_group_size: 1
    .uses_dynamic_stack: false
    .vgpr_count:     96
    .vgpr_spill_count: 0
    .wavefront_size: 64
  - .agpr_count:     0
    .args:
      - .actual_access:  read_only
        .address_space:  global
        .offset:         0
        .size:           8
        .value_kind:     global_buffer
      - .actual_access:  read_only
        .address_space:  global
        .offset:         8
        .size:           8
        .value_kind:     global_buffer
      - .actual_access:  read_only
        .address_space:  global
        .offset:         16
        .size:           8
        .value_kind:     global_buffer
      - .actual_access:  read_only
        .address_space:  global
        .offset:         24
        .size:           8
        .value_kind:     global_buffer
      - .actual_access:  read_only
        .address_space:  global
        .offset:         32
        .size:           8
        .value_kind:     global_buffer
      - .actual_access:  read_only
        .address_space:  global
        .offset:         40
        .size:           8
        .value_kind:     global_buffer
      - .actual_access:  write_only
        .address_space:  global
        .offset:         48
        .size:           8
        .value_kind:     global_buffer
      - .actual_access:  read_only
        .address_space:  global
        .offset:         56
        .size:           8
        .value_kind:     global_buffer
      - .actual_access:  read_only
        .address_space:  global
        .offset:         64
        .size:           8
        .value_kind:     global_buffer
      - .actual_access:  read_only
        .address_space:  global
        .offset:         72
        .size:           8
        .value_kind:     global_buffer
    .group_segment_fixed_size: 1024
    .kernarg_segment_align: 8
    .kernarg_segment_size: 80
    .language:       OpenCL C
    .language_version:
      - 2
      - 0
    .max_flat_workgroup_size: 256
    .name:           _Z6k_agg2PKiS0_PK6__halfPKfS5_S5_PfS5_S0_S0_
    .private_segment_fixed_size: 0
    .sgpr_count:     28
    .sgpr_spill_count: 0
    .symbol:         _Z6k_agg2PKiS0_PK6__halfPKfS5_S5_PfS5_S0_S0_.kd
    .uniform_work_group_size: 1
    .uses_dynamic_stack: false
    .vgpr_count:     60
    .vgpr_spill_count: 0
    .wavefront_size: 64
